# MLA V^T phase: the item's 8 row loads issued together up front instead of one at a time behind vmcnt(0)
# speedup vs baseline: 1.0275x; 1.0036x over previous
.LBB0_599:
	s_mov_b32 s5, 0
	v_mov_b32_e32 v192, v12
	v_ashrrev_i32_e32 v193, 31, v12
	v_lshlrev_b64 v[192:193], 11, v[192:193]
	v_lshl_add_u64 v[192:193], v[6:7], 0, v[192:193]
	s_mov_b64 s[100:101], 0x4000
	global_load_dwordx4 v[160:163], v[192:193], off offset:128
	v_lshl_add_u64 v[192:193], v[192:193], 0, s[100:101]
	global_load_dwordx4 v[164:167], v[192:193], off offset:128
	v_lshl_add_u64 v[192:193], v[192:193], 0, s[100:101]
	global_load_dwordx4 v[168:171], v[192:193], off offset:128
	v_lshl_add_u64 v[192:193], v[192:193], 0, s[100:101]
	global_load_dwordx4 v[172:175], v[192:193], off offset:128
	v_lshl_add_u64 v[192:193], v[192:193], 0, s[100:101]
	global_load_dwordx4 v[176:179], v[192:193], off offset:128
	v_lshl_add_u64 v[192:193], v[192:193], 0, s[100:101]
	global_load_dwordx4 v[180:183], v[192:193], off offset:128
	v_lshl_add_u64 v[192:193], v[192:193], 0, s[100:101]
	global_load_dwordx4 v[184:187], v[192:193], off offset:128
	v_lshl_add_u64 v[192:193], v[192:193], 0, s[100:101]
	global_load_dwordx4 v[188:191], v[192:193], off offset:128
.LBB0_600:
	v_add_u32_e32 v8, s5, v12
	v_ashrrev_i32_e32 v9, 31, v8
	v_lshlrev_b64 v[14:15], 11, v[8:9]
	v_lshl_add_u64 v[14:15], v[6:7], 0, v[14:15]
	s_waitcnt vmcnt(0)
	v_mov_b64_e32 v[14:15], v[160:161]
	v_mov_b64_e32 v[16:17], v[162:163]
	v_add_u32_e32 v1, s5, v10
	v_and_b32_e32 v9, 48, v1
	v_add_u32_e32 v9, v11, v9
	v_add_u32_e32 v1, 16, v1
	v_and_b32_e32 v1, 48, v1
	v_add_u32_e32 v1, v11, v1
	s_add_i32 s5, s5, 32
	s_cmp_eq_u32 s5, 64
	v_lshrrev_b32_e32 v13, 8, v14
	ds_write_b8 v9, v14
	ds_write_b8 v9, v13 offset:80
	ds_write_b8_d16_hi v9, v14 offset:160
	v_lshrrev_b32_e32 v13, 24, v14
	ds_write_b8 v9, v13 offset:240
	ds_write_b8 v9, v15 offset:320
	v_lshrrev_b32_e32 v13, 8, v15
	ds_write_b8 v9, v13 offset:400
	ds_write_b8_d16_hi v9, v15 offset:480
	v_lshrrev_b32_e32 v13, 24, v15
	ds_write_b8 v9, v13 offset:560
	ds_write_b8 v9, v16 offset:640
	v_lshrrev_b32_e32 v13, 8, v16
	v_add_u32_e32 v14, 8, v8
	ds_write_b8 v9, v13 offset:720
	ds_write_b8_d16_hi v9, v16 offset:800
	v_lshrrev_b32_e32 v13, 24, v16
	v_ashrrev_i32_e32 v15, 31, v14
	ds_write_b8 v9, v13 offset:880
	ds_write_b8 v9, v17 offset:960
	v_lshrrev_b32_e32 v13, 8, v17
	v_lshlrev_b64 v[14:15], 11, v[14:15]
	ds_write_b8 v9, v13 offset:1040
	ds_write_b8_d16_hi v9, v17 offset:1120
	v_lshl_add_u64 v[14:15], v[6:7], 0, v[14:15]
	v_lshrrev_b32_e32 v13, 24, v17
	v_mov_b64_e32 v[14:15], v[164:165]
	v_mov_b64_e32 v[16:17], v[166:167]
	ds_write_b8 v9, v13 offset:1200
	v_lshrrev_b32_e32 v13, 8, v14
	ds_write_b8 v9, v14 offset:8
	ds_write_b8 v9, v13 offset:88
	ds_write_b8_d16_hi v9, v14 offset:168
	v_lshrrev_b32_e32 v13, 24, v14
	ds_write_b8 v9, v13 offset:248
	ds_write_b8 v9, v15 offset:328
	v_lshrrev_b32_e32 v13, 8, v15
	ds_write_b8 v9, v13 offset:408
	ds_write_b8_d16_hi v9, v15 offset:488
	v_lshrrev_b32_e32 v13, 24, v15
	ds_write_b8 v9, v13 offset:568
	ds_write_b8 v9, v16 offset:648
	v_lshrrev_b32_e32 v13, 8, v16
	v_add_u32_e32 v14, 16, v8
	ds_write_b8 v9, v13 offset:728
	ds_write_b8_d16_hi v9, v16 offset:808
	v_lshrrev_b32_e32 v13, 24, v16
	v_ashrrev_i32_e32 v15, 31, v14
	ds_write_b8 v9, v13 offset:888
	ds_write_b8 v9, v17 offset:968
	v_lshrrev_b32_e32 v13, 8, v17
	v_lshlrev_b64 v[14:15], 11, v[14:15]
	ds_write_b8 v9, v13 offset:1048
	ds_write_b8_d16_hi v9, v17 offset:1128
	v_lshl_add_u64 v[14:15], v[6:7], 0, v[14:15]
	v_lshrrev_b32_e32 v13, 24, v17
	v_mov_b64_e32 v[14:15], v[168:169]
	v_mov_b64_e32 v[16:17], v[170:171]
	ds_write_b8 v9, v13 offset:1208
	v_add_u32_e32 v8, 24, v8
	v_lshrrev_b32_e32 v9, 8, v14
	ds_write_b8 v1, v14
	ds_write_b8 v1, v9 offset:80
	ds_write_b8_d16_hi v1, v14 offset:160
	v_lshrrev_b32_e32 v9, 24, v14
	ds_write_b8 v1, v9 offset:240
	ds_write_b8 v1, v15 offset:320
	v_lshrrev_b32_e32 v9, 8, v15
	ds_write_b8 v1, v9 offset:400
	ds_write_b8_d16_hi v1, v15 offset:480
	v_lshrrev_b32_e32 v9, 24, v15
	ds_write_b8 v1, v9 offset:560
	ds_write_b8 v1, v16 offset:640
	v_lshrrev_b32_e32 v9, 8, v16
	ds_write_b8 v1, v9 offset:720
	ds_write_b8_d16_hi v1, v16 offset:800
	v_lshrrev_b32_e32 v9, 24, v16
	ds_write_b8 v1, v9 offset:880
	ds_write_b8 v1, v17 offset:960
	v_lshrrev_b32_e32 v9, 8, v17
	ds_write_b8 v1, v9 offset:1040
	ds_write_b8_d16_hi v1, v17 offset:1120
	v_lshrrev_b32_e32 v9, 24, v17
	ds_write_b8 v1, v9 offset:1200
	v_ashrrev_i32_e32 v9, 31, v8
	v_lshlrev_b64 v[8:9], 11, v[8:9]
	v_lshl_add_u64 v[8:9], v[6:7], 0, v[8:9]
	v_mov_b64_e32 v[14:15], v[172:173]
	v_mov_b64_e32 v[16:17], v[174:175]
	v_lshrrev_b32_e32 v8, 8, v14
	ds_write_b8 v1, v14 offset:8
	ds_write_b8 v1, v8 offset:88
	ds_write_b8_d16_hi v1, v14 offset:168
	v_lshrrev_b32_e32 v8, 24, v14
	ds_write_b8 v1, v8 offset:248
	ds_write_b8 v1, v15 offset:328
	v_lshrrev_b32_e32 v8, 8, v15
	ds_write_b8 v1, v8 offset:408
	ds_write_b8_d16_hi v1, v15 offset:488
	v_lshrrev_b32_e32 v8, 24, v15
	ds_write_b8 v1, v8 offset:568
	ds_write_b8 v1, v16 offset:648
	v_lshrrev_b32_e32 v8, 8, v16
	ds_write_b8 v1, v8 offset:728
	ds_write_b8_d16_hi v1, v16 offset:808
	v_lshrrev_b32_e32 v8, 24, v16
	ds_write_b8 v1, v8 offset:888
	ds_write_b8 v1, v17 offset:968
	v_lshrrev_b32_e32 v8, 8, v17
	ds_write_b8 v1, v8 offset:1048
	ds_write_b8_d16_hi v1, v17 offset:1128
	v_lshrrev_b32_e32 v8, 24, v17
	ds_write_b8 v1, v8 offset:1208
	v_mov_b64_e32 v[160:161], v[176:177]
	v_mov_b64_e32 v[162:163], v[178:179]
	v_mov_b64_e32 v[164:165], v[180:181]
	v_mov_b64_e32 v[166:167], v[182:183]
	v_mov_b64_e32 v[168:169], v[184:185]
	v_mov_b64_e32 v[170:171], v[186:187]
	v_mov_b64_e32 v[172:173], v[188:189]
	v_mov_b64_e32 v[174:175], v[190:191]
	s_cbranch_scc0 .LBB0_600
	s_ashr_i32 s2, s12, 31
	s_bfe_i32 s5, s12, 0x10019
	s_lshl_b32 s3, s12, 6
	s_lshr_b32 s2, s2, 25
	s_lshr_b32 s5, s5, 19
	s_add_i32 s2, s12, s2
	s_add_i32 s5, s3, s5
	s_ashr_i32 s2, s2, 7
	s_and_b32 s5, s5, 0xffffe000
	s_sub_i32 s5, s3, s5
	s_ashr_i32 s3, s2, 31
	s_lshl_b64 s[2:3], s[2:3], 23
	s_add_u32 s2, s0, s2
	s_addc_u32 s3, s1, s3
	s_ashr_i32 s6, s5, 31
	s_add_u32 s2, s2, s5
	s_addc_u32 s3, s3, s6
	v_lshl_add_u64 v[8:9], s[2:3], 0, v[2:3]
	s_mov_b32 s2, 0
	s_waitcnt lgkmcnt(0)
	s_barrier
